# baseline (speedup 1.0000x reference)
.LBB1_4:
	global_load_dwordx4 v[30:33], v[4:5], off
	v_add_u32_e32 v3, s18, v3
	v_cmp_lt_u32_e64 s[2:3], s19, v3
	v_lshl_add_u64 v[4:5], v[4:5], 0, s[16:17]
	s_or_b64 s[4:5], s[2:3], s[4:5]
	s_waitcnt vmcnt(0)
	ds_write_b128 v2, v[30:33]
	v_add_u32_e32 v2, s16, v2
	s_andn2_b64 exec, exec, s[4:5]
	s_cbranch_execnz .LBB1_4
	s_or_b64 exec, exec, s[4:5]
	s_waitcnt lgkmcnt(0)
	s_barrier
	s_and_saveexec_b64 s[2:3], vcc
	s_cbranch_execz .LBB1_8
	v_lshlrev_b32_e32 v2, 2, v0
	v_lshrrev_b32_e32 v3, 4, v29
	v_lshlrev_b32_e32 v104, 4, v29
	v_and_or_b32 v2, v2, 60, v3
	s_mov_b32 s4, 0x5040100
	v_lshlrev_b32_e32 v105, 2, v2
	v_perm_b32 v2, v26, v25, s4
	v_alignbit_b32 v3, v27, v26, 16
	v_alignbit_b32 v4, v28, v27, 16
	v_alignbit_b32 v5, v24, v28, 16
	ds_read_b128 v[24:27], v104
	ds_bpermute_b32 v2, v105, v2
	ds_bpermute_b32 v3, v105, v3
	ds_bpermute_b32 v4, v105, v4
	ds_bpermute_b32 v5, v105, v5
	ds_read_b128 v[28:31], v104 offset:4096
	ds_read_b128 v[32:35], v104 offset:1024
	ds_read_b128 v[36:39], v104 offset:8192
	ds_read_b128 v[40:43], v104 offset:5120
	ds_read_b128 v[44:47], v104 offset:12288
	ds_read_b128 v[48:51], v104 offset:16384
	ds_read_b128 v[52:55], v104 offset:9216
	v_perm_b32 v20, v23, v20, s4
	v_alignbit_b32 v23, v22, v23, 16
	v_alignbit_b32 v22, v21, v22, 16
	v_alignbit_b32 v19, v19, v21, 16
	ds_read_b128 v[56:59], v104 offset:20480
	ds_read_b128 v[60:63], v104 offset:13312
	ds_read_b128 v[64:67], v104 offset:24576
	ds_read_b128 v[68:71], v104 offset:17408
	ds_bpermute_b32 v20, v105, v20
	ds_bpermute_b32 v21, v105, v23
	ds_bpermute_b32 v22, v105, v22
	ds_bpermute_b32 v23, v105, v19
	s_waitcnt lgkmcnt(14)
	v_mfma_f32_16x16x32_f16 v[24:27], v[24:27], v[2:5], 0
	ds_read_b128 v[72:75], v104 offset:28672
	ds_read_b128 v[76:79], v104 offset:21504
	ds_read_b128 v[80:83], v104 offset:25600
	ds_read_b128 v[84:87], v104 offset:29696
	v_mfma_f32_16x16x32_f16 v[28:31], v[28:31], v[2:5], 0
	v_lshlrev_b32_e32 v19, 1, v0
	v_and_b32_e32 v106, 0x60, v19
	v_perm_b32 v15, v16, v15, s4
	s_waitcnt lgkmcnt(14)
	v_mfma_f32_16x16x32_f16 v[36:39], v[36:39], v[2:5], 0
	v_alignbit_b32 v16, v17, v16, 16
	v_alignbit_b32 v17, v18, v17, 16
	v_alignbit_b32 v18, v14, v18, 16
	v_mfma_f32_16x16x32_f16 v[44:47], v[44:47], v[2:5], 0
	ds_bpermute_b32 v14, v105, v15
	ds_bpermute_b32 v15, v105, v16
	ds_bpermute_b32 v16, v105, v17
	s_waitcnt lgkmcnt(14)
	v_mfma_f32_16x16x32_f16 v[48:51], v[48:51], v[2:5], 0
	ds_bpermute_b32 v17, v105, v18
	v_perm_b32 v13, v12, v13, s4
	v_alignbit_b32 v12, v11, v12, 16
	s_waitcnt lgkmcnt(8)
	v_mfma_f32_16x16x32_f16 v[24:27], v[32:35], v[20:23], v[24:27]
	v_alignbit_b32 v11, v10, v11, 16
	v_alignbit_b32 v7, v7, v10, 16
	v_lshlrev_b32_e32 v6, 4, v6
	v_mfma_f32_16x16x32_f16 v[28:31], v[40:43], v[20:23], v[28:31]
	v_lshlrev_b32_e32 v8, 4, v8
	s_movk_i32 s4, 0xc0
	v_and_b32_e32 v10, 15, v0
	v_mfma_f32_16x16x32_f16 v[32:35], v[52:55], v[20:23], v[36:39]
	v_cmp_gt_u32_e32 vcc, 10, v10
	v_mfma_f32_16x16x32_f16 v[36:39], v[60:63], v[20:23], v[44:47]
	v_mfma_f32_16x16x32_f16 v[40:43], v[68:71], v[20:23], v[48:51]
	s_nop 2
	global_load_dwordx4 v[48:51], v106, s[6:7] offset:16
	global_load_dwordx4 v[52:55], v106, s[6:7]
	ds_read_b128 v[60:63], v104 offset:2048
	v_mfma_f32_16x16x32_f16 v[56:59], v[56:59], v[2:5], 0
	v_mfma_f32_16x16x32_f16 v[64:67], v[64:67], v[2:5], 0
	s_waitcnt lgkmcnt(8)
	v_mfma_f32_16x16x32_f16 v[2:5], v[72:75], v[2:5], 0
	s_waitcnt lgkmcnt(7)
	v_mfma_f32_16x16x32_f16 v[44:47], v[76:79], v[20:23], v[56:59]
	s_waitcnt lgkmcnt(6)
	v_mfma_f32_16x16x32_f16 v[56:59], v[80:83], v[20:23], v[64:67]
	s_waitcnt lgkmcnt(5)
	v_mfma_f32_16x16x32_f16 v[2:5], v[84:87], v[20:23], v[2:5]
	ds_read_b128 v[18:21], v104 offset:6144
	ds_read_b128 v[64:67], v104 offset:10240
	ds_read_b128 v[68:71], v104 offset:3072
	s_waitcnt lgkmcnt(3)
	v_mfma_f32_16x16x32_f16 v[22:25], v[60:63], v[14:17], v[24:27]
	ds_read_b128 v[60:63], v104 offset:14336
	ds_read_b128 v[72:75], v104 offset:7168
	s_waitcnt lgkmcnt(4)
	v_mfma_f32_16x16x32_f16 v[18:21], v[18:21], v[14:17], v[28:31]
	s_nop 2
	ds_read_b128 v[26:29], v104 offset:18432
	ds_read_b128 v[76:79], v104 offset:22528
	ds_read_b128 v[80:83], v104 offset:11264
	s_waitcnt lgkmcnt(6)
	v_mfma_f32_16x16x32_f16 v[30:33], v[64:67], v[14:17], v[32:35]
	ds_read_b128 v[64:67], v104 offset:15360
	global_load_dwordx4 v[84:87], v106, s[6:7] offset:144
	global_load_dwordx4 v[88:91], v106, s[6:7] offset:128
	s_waitcnt lgkmcnt(3)
	v_mfma_f32_16x16x32_f16 v[26:29], v[26:29], v[14:17], v[40:43]
	s_waitcnt lgkmcnt(2)
	v_mfma_f32_16x16x32_f16 v[42:45], v[76:79], v[14:17], v[44:47]
	ds_bpermute_b32 v76, v105, v13
	ds_bpermute_b32 v77, v105, v12
	ds_bpermute_b32 v78, v105, v11
	ds_bpermute_b32 v79, v105, v7
	v_mfma_f32_16x16x32_f16 v[34:37], v[60:63], v[14:17], v[36:39]
	ds_read_b128 v[60:63], v104 offset:26624
	ds_read_b128 v[92:95], v104 offset:19456
	s_nop 0
	ds_read_b128 v[38:41], v104 offset:30720
	ds_read_b128 v[96:99], v104 offset:23552
	ds_read_b128 v[100:103], v104 offset:27648
	s_waitcnt lgkmcnt(4)
	v_mfma_f32_16x16x32_f16 v[56:59], v[60:63], v[14:17], v[56:59]
	ds_read_b128 v[60:63], v104 offset:31744
	v_mov_b32_e32 v7, 0
	s_waitcnt lgkmcnt(3)
	v_mfma_f32_16x16x32_f16 v[2:5], v[38:41], v[14:17], v[2:5]
	global_load_dwordx4 v[38:41], v106, s[6:7] offset:272
	v_mfma_f32_16x16x32_f16 v[12:15], v[68:71], v[76:79], v[22:25]
	s_nop 2
	global_load_dwordx4 v[22:25], v106, s[6:7] offset:256
	v_mfma_f32_16x16x32_f16 v[34:37], v[64:67], v[76:79], v[34:37]
	global_load_dwordx4 v[64:67], v106, s[6:7] offset:400
	global_load_dwordx4 v[68:71], v106, s[6:7] offset:384
	s_waitcnt vmcnt(6)
	v_pk_add_f32 v[12:13], v[12:13], v[52:53]
	v_mfma_f32_16x16x32_f16 v[16:19], v[72:75], v[76:79], v[18:21]
	v_lshl_add_u64 v[72:73], s[10:11], 0, v[6:7]
	v_lshlrev_b32_e32 v6, 1, v9
	v_pk_add_f32 v[14:15], v[14:15], v[54:55]
	v_lshl_add_u64 v[20:21], s[8:9], 0, v[6:7]
	v_lshlrev_b32_e32 v6, 6, v0
	v_and_b32_e32 v9, 60, v0
	v_cvt_pk_f16_f32 v12, v12, v13
	v_cvt_pk_f16_f32 v13, v14, v15
	v_pk_add_f32 v[14:15], v[16:17], v[48:49]
	v_pk_add_f32 v[16:17], v[18:19], v[50:51]
	v_or_b32_e32 v54, v8, v1
	v_and_or_b32 v6, v6, s4, v9
	v_cvt_pk_f16_f32 v14, v14, v15
	v_cvt_pk_f16_f32 v15, v16, v17
	v_ashrrev_i32_e32 v55, 31, v54
	ds_bpermute_b32 v16, v6, v12
	ds_bpermute_b32 v17, v6, v13
	ds_bpermute_b32 v18, v6, v14
	ds_bpermute_b32 v19, v6, v15
	v_lshlrev_b64 v[46:47], 8, v[54:55]
	v_mfma_f32_16x16x32_f16 v[30:33], v[80:83], v[76:79], v[30:33]
	v_lshl_add_u64 v[74:75], v[20:21], 0, v[46:47]
	global_load_dwordx4 v[46:49], v104, s[12:13]
	global_load_dwordx4 v[50:53], v104, s[12:13] offset:1024
	v_mfma_f32_16x16x32_f16 v[26:29], v[92:95], v[76:79], v[26:29]
	s_waitcnt lgkmcnt(0)
	global_store_dwordx4 v[74:75], v[16:19], off
	v_cvt_f32_f16_e32 v9, v16
	v_cvt_f32_f16_sdwa v11, v16 dst_sel:DWORD dst_unused:UNUSED_PAD src0_sel:WORD_1
	v_mfma_f32_16x16x32_f16 v[42:45], v[96:99], v[76:79], v[42:45]
	v_cvt_f32_f16_e32 v80, v19
	v_cvt_f32_f16_sdwa v81, v19 dst_sel:DWORD dst_unused:UNUSED_PAD src0_sel:WORD_1
	s_waitcnt vmcnt(5)
	v_pk_add_f32 v[20:21], v[26:27], v[22:23]
	v_mfma_f32_16x16x32_f16 v[56:59], v[100:103], v[76:79], v[56:59]
	v_add_f32_e64 v22, v28, v24
	v_add_f32_e64 v23, v29, v25
	v_cvt_pk_f16_f32 v20, v20, v21
	v_cvt_pk_f16_f32 v21, v22, v23
	v_mfma_f32_16x16x32_f16 v[2:5], v[60:63], v[76:79], v[2:5]
	v_cvt_f32_f16_e32 v76, v17
	v_cvt_f32_f16_sdwa v77, v17 dst_sel:DWORD dst_unused:UNUSED_PAD src0_sel:WORD_1
	v_pk_add_f32 v[16:17], v[30:31], v[88:89]
	v_cvt_f32_f16_e32 v78, v18
	v_cvt_pk_f16_f32 v30, v16, v17
	v_pk_add_f32 v[16:17], v[32:33], v[90:91]
	v_cvt_f32_f16_sdwa v79, v18 dst_sel:DWORD dst_unused:UNUSED_PAD src0_sel:WORD_1
	v_cvt_pk_f16_f32 v31, v16, v17
	v_pk_add_f32 v[16:17], v[34:35], v[84:85]
	global_load_dwordx4 v[60:63], v104, s[12:13] offset:3072
	v_cvt_pk_f16_f32 v32, v16, v17
	v_pk_add_f32 v[16:17], v[36:37], v[86:87]
	v_pk_add_f32 v[22:23], v[42:43], v[38:39]
	v_cvt_pk_f16_f32 v33, v16, v17
	global_load_dwordx4 v[16:19], v104, s[12:13] offset:2048
	v_pk_add_f32 v[24:25], v[44:45], v[40:41]
	v_cvt_pk_f16_f32 v22, v22, v23
	v_cvt_pk_f16_f32 v23, v24, v25
	ds_bpermute_b32 v24, v6, v20
	ds_bpermute_b32 v25, v6, v21
	ds_bpermute_b32 v26, v6, v22
	ds_bpermute_b32 v27, v6, v23
	ds_bpermute_b32 v34, v6, v30
	ds_bpermute_b32 v35, v6, v31
	ds_bpermute_b32 v36, v6, v32
	ds_bpermute_b32 v37, v6, v33
	s_waitcnt lgkmcnt(4)
	global_store_dwordx4 v[74:75], v[24:27], off offset:128
	v_cvt_f32_f16_e32 v40, v24
	v_cvt_f32_f16_sdwa v41, v24 dst_sel:DWORD dst_unused:UNUSED_PAD src0_sel:WORD_1
	v_cvt_f32_f16_e32 v42, v25
	v_cvt_f32_f16_sdwa v43, v25 dst_sel:DWORD dst_unused:UNUSED_PAD src0_sel:WORD_1
	s_waitcnt vmcnt(6)
	v_pk_add_f32 v[24:25], v[56:57], v[68:69]
	v_pk_add_f32 v[2:3], v[2:3], v[64:65]
	s_waitcnt lgkmcnt(0)
	global_store_dwordx4 v[74:75], v[34:37], off offset:64
	v_cvt_f32_f16_e32 v82, v34
	v_cvt_f32_f16_sdwa v83, v34 dst_sel:DWORD dst_unused:UNUSED_PAD src0_sel:WORD_1
	v_cvt_f32_f16_e32 v28, v36
	v_cvt_f32_f16_sdwa v29, v36 dst_sel:DWORD dst_unused:UNUSED_PAD src0_sel:WORD_1
	v_cvt_pk_f16_f32 v34, v24, v25
	v_pk_add_f32 v[24:25], v[58:59], v[70:71]
	v_cvt_pk_f16_f32 v36, v2, v3
	v_pk_add_f32 v[2:3], v[4:5], v[66:67]
	v_cvt_f32_f16_e32 v84, v35
	v_cvt_f32_f16_sdwa v85, v35 dst_sel:DWORD dst_unused:UNUSED_PAD src0_sel:WORD_1
	v_cvt_f32_f16_e32 v38, v37
	v_cvt_f32_f16_sdwa v39, v37 dst_sel:DWORD dst_unused:UNUSED_PAD src0_sel:WORD_1
	v_cvt_pk_f16_f32 v35, v24, v25
	v_cvt_pk_f16_f32 v37, v2, v3
	ds_bpermute_b32 v2, v6, v34
	ds_bpermute_b32 v3, v6, v35
	ds_bpermute_b32 v4, v6, v36
	ds_bpermute_b32 v5, v6, v37
	v_cvt_f32_f16_e32 v6, v26
	v_cvt_f32_f16_sdwa v26, v26 dst_sel:DWORD dst_unused:UNUSED_PAD src0_sel:WORD_1
	v_cvt_f32_f16_e32 v44, v27
	v_cvt_f32_f16_sdwa v45, v27 dst_sel:DWORD dst_unused:UNUSED_PAD src0_sel:WORD_1
	s_waitcnt lgkmcnt(0)
	global_store_dwordx4 v[74:75], v[2:5], off offset:192
	v_cvt_f32_f16_e32 v27, v2
	v_cvt_f32_f16_sdwa v56, v2 dst_sel:DWORD dst_unused:UNUSED_PAD src0_sel:WORD_1
	v_mov_b32_e32 v2, v7
	s_waitcnt vmcnt(7)
	v_mfma_f32_16x16x32_f16 v[12:15], v[12:15], v[46:49], 0
	v_cvt_f32_f16_e32 v59, v4
	v_cvt_pk_fp8_f32 v2, v9, v11
	v_cvt_f32_f16_sdwa v9, v4 dst_sel:DWORD dst_unused:UNUSED_PAD src0_sel:WORD_1
	v_mov_b32_e32 v25, v7
	v_cvt_f32_f16_e32 v57, v3
	v_cvt_f32_f16_sdwa v58, v3 dst_sel:DWORD dst_unused:UNUSED_PAD src0_sel:WORD_1
	v_cvt_f32_f16_e32 v11, v5
	v_cvt_f32_f16_sdwa v64, v5 dst_sel:DWORD dst_unused:UNUSED_PAD src0_sel:WORD_1
	v_mov_b32_e32 v3, v7
	v_mov_b32_e32 v4, v7
	v_mov_b32_e32 v5, v7
	v_cvt_pk_fp8_f32 v25, v6, v26
	v_mov_b32_e32 v26, v7
	v_cvt_pk_fp8_f32 v3, v78, v79
	v_cvt_pk_fp8_f32 v4, v82, v83
	v_cvt_pk_fp8_f32 v5, v28, v29
	v_mov_b32_e32 v24, v7
	v_cvt_pk_fp8_f32 v26, v27, v56
	v_mov_b32_e32 v27, v7
	s_waitcnt vmcnt(6)
	v_mfma_f32_16x16x32_f16 v[12:15], v[30:33], v[50:53], v[12:15]
	v_cvt_pk_fp8_f32 v24, v40, v41
	v_cvt_pk_fp8_f32 v27, v59, v9
	v_cvt_pk_fp8_f32 v2, v76, v77 op_sel:[0,0,1]
	v_cvt_pk_fp8_f32 v3, v80, v81 op_sel:[0,0,1]
	v_cvt_pk_fp8_f32 v4, v84, v85 op_sel:[0,0,1]
	v_cvt_pk_fp8_f32 v5, v38, v39 op_sel:[0,0,1]
	s_waitcnt vmcnt(3)
	v_mfma_f32_16x16x32_f16 v[12:15], v[20:23], v[16:19], v[12:15]
	v_cvt_pk_fp8_f32 v24, v42, v43 op_sel:[0,0,1]
	v_cvt_pk_fp8_f32 v25, v44, v45 op_sel:[0,0,1]
	v_cvt_pk_fp8_f32 v26, v57, v58 op_sel:[0,0,1]
	v_cvt_pk_fp8_f32 v27, v11, v64 op_sel:[0,0,1]
	v_lshlrev_b64 v[28:29], 7, v[54:55]
	v_lshl_add_u64 v[16:17], v[72:73], 0, v[28:29]
	global_store_dwordx4 v[16:17], v[2:5], off
	global_store_dwordx4 v[16:17], v[24:27], off offset:64
	s_nop 0
	v_mfma_f32_16x16x32_f16 v[2:5], v[34:37], v[60:63], v[12:15]
	s_and_b64 exec, exec, vcc
	s_cbranch_execz .LBB1_8
	v_lshlrev_b32_e32 v6, 4, v10
	v_lshlrev_b32_e32 v6, 1, v6
	v_and_b32_e32 v1, 12, v1
	v_lshl_add_u64 v[10:11], s[14:15], 0, v[6:7]
	v_lshlrev_b32_e32 v6, 1, v1
	v_lshl_add_u64 v[6:7], v[10:11], 0, v[6:7]
	v_mul_u32_u24_e32 v8, 10, v8
	v_ashrrev_i32_e32 v9, 31, v8
	v_lshl_add_u64 v[6:7], v[8:9], 1, v[6:7]
	v_cvt_pk_f16_f32 v5, v4, v5
	v_cvt_pk_f16_f32 v4, v2, v3
	global_store_dwordx2 v[6:7], v[4:5], off

.LBB5_6:
	s_or_b64 exec, exec, s[16:17]
	v_mov_b32_e32 v29, 0
	v_and_b32_e32 v0, 15, v0
	v_lshrrev_b32_e32 v27, 4, v71
	s_waitcnt lgkmcnt(0)
	v_lshl_add_u64 v[84:85], s[8:9], 0, v[28:29]
	v_lshlrev_b32_e32 v28, 4, v71
	v_cmp_gt_u32_e32 vcc, 10, v0
	v_lshlrev_b32_e32 v0, 4, v0
	v_and_or_b32 v26, v26, 60, v27
	v_lshl_add_u64 v[88:89], s[10:11], 0, v[28:29]
	v_lshlrev_b32_e32 v28, 1, v0
	v_and_b32_e32 v0, 12, v94
	v_lshlrev_b32_e32 v70, 3, v70
	v_lshlrev_b32_e32 v95, 2, v26
	v_lshl_add_u64 v[26:27], s[6:7], 0, v[28:29]
	v_lshlrev_b32_e32 v28, 1, v0
	v_lshl_add_u64 v[86:87], v[26:27], 0, v[28:29]
	v_lshlrev_b32_e32 v96, 2, v70
	s_barrier
	s_and_saveexec_b64 s[0:1], s[2:3]
	s_cbranch_execz .LBB5_9
	v_lshlrev_b32_e32 v0, 4, v1
	ds_read_b128 v[70:73], v96
	ds_read_b128 v[74:77], v96 offset:512
	v_or_b32_e32 v90, v0, v94
	v_ashrrev_i32_e32 v91, 31, v90
	v_lshlrev_b64 v[26:27], 8, v[90:91]
	v_lshl_add_u64 v[92:93], v[82:83], 0, v[26:27]
	s_waitcnt vmcnt(5)
	v_cvt_f32_f16_sdwa v27, v66 dst_sel:DWORD dst_unused:UNUSED_PAD src0_sel:WORD_1
	v_cvt_f32_f16_e32 v26, v66
	s_waitcnt lgkmcnt(0)
	v_fma_mix_f32 v1, v70, v62, v74 op_sel_hi:[0,1,0]
	v_max_f32_e32 v70, 0, v1
	v_fma_mix_f32 v1, v71, v62, v75 op_sel:[0,1,0] op_sel_hi:[0,1,0]
	v_max_f32_e32 v71, 0, v1
	ds_read_b128 v[78:81], v96 offset:16
	ds_read_b128 v[98:101], v96 offset:528
	v_pk_add_f32 v[26:27], v[70:71], v[26:27]
	v_cvt_f32_f16_sdwa v71, v67 dst_sel:DWORD dst_unused:UNUSED_PAD src0_sel:WORD_1
	v_cvt_f32_f16_e32 v70, v67
	v_fma_mix_f32 v1, v72, v63, v76 op_sel_hi:[0,1,0]
	v_max_f32_e32 v62, 0, v1
	v_fma_mix_f32 v1, v73, v63, v77 op_sel:[0,1,0] op_sel_hi:[0,1,0]
	v_max_f32_e32 v63, 0, v1
	v_pk_add_f32 v[70:71], v[62:63], v[70:71]
	v_cvt_f32_f16_sdwa v63, v68 dst_sel:DWORD dst_unused:UNUSED_PAD src0_sel:WORD_1
	v_cvt_f32_f16_e32 v62, v68
	s_waitcnt lgkmcnt(0)
	v_fma_mix_f32 v1, v78, v64, v98 op_sel_hi:[0,1,0]
	v_max_f32_e32 v72, 0, v1
	v_fma_mix_f32 v1, v79, v64, v99 op_sel:[0,1,0] op_sel_hi:[0,1,0]
	v_cvt_f32_f16_sdwa v75, v69 dst_sel:DWORD dst_unused:UNUSED_PAD src0_sel:WORD_1
	v_cvt_f32_f16_e32 v74, v69
	v_max_f32_e32 v73, 0, v1
	v_fma_mix_f32 v1, v80, v65, v100 op_sel_hi:[0,1,0]
	v_pk_add_f32 v[72:73], v[72:73], v[62:63]
	v_max_f32_e32 v64, 0, v1
	v_fma_mix_f32 v1, v81, v65, v101 op_sel:[0,1,0] op_sel_hi:[0,1,0]
	v_mov_b32_e32 v62, v29
	v_max_f32_e32 v65, 0, v1
	v_cvt_pk_fp8_f32 v62, v26, v27
	v_cvt_pk_f16_f32 v66, v26, v27
	v_pk_add_f32 v[26:27], v[64:65], v[74:75]
	v_cvt_pk_f16_f32 v67, v70, v71
	v_cvt_pk_f16_f32 v68, v72, v73
	v_cvt_pk_f16_f32 v69, v26, v27
	v_mov_b32_e32 v63, v29
	global_store_dwordx4 v[92:93], v[66:69], off
	v_cvt_pk_fp8_f32 v63, v72, v73
	v_cvt_pk_fp8_f32 v62, v70, v71 op_sel:[0,0,1]
	ds_read_b128 v[70:73], v96 offset:128
	ds_read_b128 v[74:77], v96 offset:640
	ds_read_b128 v[78:81], v96 offset:144
	ds_read_b128 v[98:101], v96 offset:656
	v_cvt_pk_fp8_f32 v63, v26, v27 op_sel:[0,0,1]
	s_waitcnt vmcnt(5)
	v_cvt_f32_f16_sdwa v27, v58 dst_sel:DWORD dst_unused:UNUSED_PAD src0_sel:WORD_1
	v_cvt_f32_f16_e32 v26, v58
	s_waitcnt lgkmcnt(2)
	v_fma_mix_f32 v1, v70, v54, v74 op_sel_hi:[0,1,0]
	v_max_f32_e32 v64, 0, v1
	v_fma_mix_f32 v1, v71, v54, v75 op_sel:[0,1,0] op_sel_hi:[0,1,0]
	v_max_f32_e32 v65, 0, v1
	v_pk_add_f32 v[26:27], v[64:65], v[26:27]
	v_cvt_f32_f16_sdwa v65, v59 dst_sel:DWORD dst_unused:UNUSED_PAD src0_sel:WORD_1
	v_cvt_f32_f16_e32 v64, v59
	v_fma_mix_f32 v1, v72, v55, v76 op_sel_hi:[0,1,0]
	v_max_f32_e32 v58, 0, v1
	v_fma_mix_f32 v1, v73, v55, v77 op_sel:[0,1,0] op_sel_hi:[0,1,0]
	v_max_f32_e32 v59, 0, v1
	v_pk_add_f32 v[58:59], v[58:59], v[64:65]
	v_cvt_f32_f16_sdwa v65, v60 dst_sel:DWORD dst_unused:UNUSED_PAD src0_sel:WORD_1
	v_cvt_f32_f16_e32 v64, v60
	s_waitcnt lgkmcnt(0)
	v_fma_mix_f32 v1, v78, v56, v98 op_sel_hi:[0,1,0]
	v_max_f32_e32 v70, 0, v1
	v_fma_mix_f32 v1, v79, v56, v99 op_sel:[0,1,0] op_sel_hi:[0,1,0]
	v_cvt_f32_f16_sdwa v75, v61 dst_sel:DWORD dst_unused:UNUSED_PAD src0_sel:WORD_1
	v_cvt_f32_f16_e32 v74, v61
	v_max_f32_e32 v71, 0, v1
	v_fma_mix_f32 v1, v80, v57, v100 op_sel_hi:[0,1,0]
	v_pk_add_f32 v[70:71], v[70:71], v[64:65]
	v_max_f32_e32 v72, 0, v1
	v_fma_mix_f32 v1, v81, v57, v101 op_sel:[0,1,0] op_sel_hi:[0,1,0]
	v_mov_b32_e32 v64, v29
	v_max_f32_e32 v73, 0, v1
	v_cvt_pk_fp8_f32 v64, v26, v27
	v_cvt_pk_f16_f32 v54, v26, v27
	v_pk_add_f32 v[26:27], v[72:73], v[74:75]
	v_cvt_pk_f16_f32 v55, v58, v59
	v_cvt_pk_f16_f32 v56, v70, v71
	v_cvt_pk_f16_f32 v57, v26, v27
	v_mov_b32_e32 v65, v29
	global_store_dwordx4 v[92:93], v[54:57], off offset:64
	v_cvt_pk_fp8_f32 v65, v70, v71
	v_cvt_pk_fp8_f32 v64, v58, v59 op_sel:[0,0,1]
	ds_read_b128 v[58:61], v96 offset:256
	ds_read_b128 v[70:73], v96 offset:768
	ds_read_b128 v[74:77], v96 offset:272
	ds_read_b128 v[78:81], v96 offset:784
	global_load_dwordx4 v[98:101], v[88:89], off
	global_load_dwordx4 v[102:105], v[88:89], off offset:1024
	v_cvt_pk_fp8_f32 v65, v26, v27 op_sel:[0,0,1]
	s_waitcnt vmcnt(5)
	v_cvt_f32_f16_sdwa v27, v50 dst_sel:DWORD dst_unused:UNUSED_PAD src0_sel:WORD_1
	v_cvt_f32_f16_e32 v26, v50
	s_waitcnt lgkmcnt(2)
	v_fma_mix_f32 v1, v58, v46, v70 op_sel_hi:[0,1,0]
	v_max_f32_e32 v58, 0, v1
	v_fma_mix_f32 v1, v59, v46, v71 op_sel:[0,1,0] op_sel_hi:[0,1,0]
	v_max_f32_e32 v59, 0, v1
	v_fma_mix_f32 v1, v60, v47, v72 op_sel_hi:[0,1,0]
	v_pk_add_f32 v[58:59], v[58:59], v[26:27]
	v_max_f32_e32 v26, 0, v1
	v_cvt_f32_f16_sdwa v107, v51 dst_sel:DWORD dst_unused:UNUSED_PAD src0_sel:WORD_1
	v_cvt_f32_f16_e32 v106, v51
	v_fma_mix_f32 v1, v61, v47, v73 op_sel:[0,1,0] op_sel_hi:[0,1,0]
	global_load_dwordx4 v[70:73], v[88:89], off offset:2048
	v_max_f32_e32 v27, 0, v1
	v_pk_add_f32 v[50:51], v[26:27], v[106:107]
	global_load_dwordx4 v[106:109], v[88:89], off offset:3072
	s_waitcnt lgkmcnt(0)
	v_fma_mix_f32 v1, v74, v48, v78 op_sel_hi:[0,1,0]
	v_cvt_f32_f16_sdwa v27, v52 dst_sel:DWORD dst_unused:UNUSED_PAD src0_sel:WORD_1
	v_cvt_f32_f16_e32 v26, v52
	v_max_f32_e32 v60, 0, v1
	v_fma_mix_f32 v1, v75, v48, v79 op_sel:[0,1,0] op_sel_hi:[0,1,0]
	v_max_f32_e32 v61, 0, v1
	v_fma_mix_f32 v1, v76, v49, v80 op_sel_hi:[0,1,0]
	v_max_f32_e32 v74, 0, v1
	v_fma_mix_f32 v1, v77, v49, v81 op_sel:[0,1,0] op_sel_hi:[0,1,0]
	v_cvt_f32_f16_sdwa v77, v53 dst_sel:DWORD dst_unused:UNUSED_PAD src0_sel:WORD_1
	v_cvt_f32_f16_e32 v76, v53
	v_pk_add_f32 v[60:61], v[60:61], v[26:27]
	v_mov_b32_e32 v26, v29
	v_mov_b32_e32 v27, v29
	v_max_f32_e32 v75, 0, v1
	v_cvt_pk_fp8_f32 v26, v58, v59
	v_cvt_pk_fp8_f32 v27, v60, v61
	v_pk_add_f32 v[52:53], v[74:75], v[76:77]
	v_cvt_pk_f16_f32 v46, v58, v59
	v_cvt_pk_f16_f32 v47, v50, v51
	v_cvt_pk_f16_f32 v48, v60, v61
	v_cvt_pk_f16_f32 v49, v52, v53
	global_store_dwordx4 v[92:93], v[46:49], off offset:128
	v_cvt_pk_fp8_f32 v26, v50, v51 op_sel:[0,0,1]
	v_cvt_pk_fp8_f32 v27, v52, v53 op_sel:[0,0,1]
	ds_read_b128 v[50:53], v96 offset:384
	ds_read_b128 v[58:61], v96 offset:896
	ds_read_b128 v[74:77], v96 offset:400
	ds_read_b128 v[78:81], v96 offset:912
	ds_bpermute_b32 v66, v95, v66
	ds_bpermute_b32 v67, v95, v67
	ds_bpermute_b32 v68, v95, v68
	s_waitcnt lgkmcnt(5)
	v_fma_mix_f32 v1, v50, v30, v58 op_sel_hi:[0,1,0]
	ds_bpermute_b32 v69, v95, v69
	v_max_f32_e32 v50, 0, v1
	v_fma_mix_f32 v1, v51, v30, v59 op_sel:[0,1,0] op_sel_hi:[0,1,0]
	s_waitcnt vmcnt(7)
	v_cvt_f32_f16_sdwa v59, v35 dst_sel:DWORD dst_unused:UNUSED_PAD src0_sel:WORD_1
	v_cvt_f32_f16_e32 v58, v35
	v_max_f32_e32 v51, 0, v1
	v_fma_mix_f32 v1, v52, v31, v60 op_sel_hi:[0,1,0]
	v_cvt_f32_f16_sdwa v111, v34 dst_sel:DWORD dst_unused:UNUSED_PAD src0_sel:WORD_1
	v_cvt_f32_f16_e32 v110, v34
	v_max_f32_e32 v34, 0, v1
	v_fma_mix_f32 v1, v53, v31, v61 op_sel:[0,1,0] op_sel_hi:[0,1,0]
	v_cvt_f32_f16_sdwa v53, v36 dst_sel:DWORD dst_unused:UNUSED_PAD src0_sel:WORD_1
	v_cvt_f32_f16_e32 v52, v36
	v_max_f32_e32 v35, 0, v1
	s_waitcnt lgkmcnt(4)
	v_fma_mix_f32 v1, v74, v32, v78 op_sel_hi:[0,1,0]
	ds_bpermute_b32 v54, v95, v54
	ds_bpermute_b32 v55, v95, v55
	ds_bpermute_b32 v56, v95, v56
	ds_bpermute_b32 v57, v95, v57
	v_pk_add_f32 v[34:35], v[34:35], v[58:59]
	v_max_f32_e32 v58, 0, v1
	v_fma_mix_f32 v1, v75, v32, v79 op_sel:[0,1,0] op_sel_hi:[0,1,0]
	v_max_f32_e32 v59, 0, v1
	v_pk_add_f32 v[52:53], v[58:59], v[52:53]
	v_cvt_f32_f16_sdwa v59, v37 dst_sel:DWORD dst_unused:UNUSED_PAD src0_sel:WORD_1
	v_cvt_f32_f16_e32 v58, v37
	v_pk_add_f32 v[50:51], v[50:51], v[110:111]
	v_fma_mix_f32 v1, v76, v33, v80 op_sel_hi:[0,1,0]
	v_mov_b32_e32 v28, v29
	ds_bpermute_b32 v46, v95, v46
	ds_bpermute_b32 v47, v95, v47
	ds_bpermute_b32 v48, v95, v48
	ds_bpermute_b32 v49, v95, v49
	v_max_f32_e32 v36, 0, v1
	v_fma_mix_f32 v1, v77, v33, v81 op_sel:[0,1,0] op_sel_hi:[0,1,0]
	v_cvt_pk_fp8_f32 v28, v50, v51
	v_cvt_pk_f16_f32 v30, v50, v51
	v_cvt_pk_f16_f32 v32, v52, v53
	v_max_f32_e32 v37, 0, v1
	v_cvt_pk_fp8_f32 v29, v52, v53
	s_waitcnt vmcnt(4) lgkmcnt(8)
	v_mfma_f32_16x16x32_f16 v[50:53], v[66:69], v[98:101], 0
	v_add_f32_e64 v58, v36, v58
	v_add_f32_e64 v59, v37, v59
	v_cvt_pk_f16_f32 v31, v34, v35
	v_cvt_pk_f16_f32 v33, v58, v59
	v_cvt_pk_fp8_f32 v28, v34, v35 op_sel:[0,0,1]
	ds_bpermute_b32 v34, v95, v30
	ds_bpermute_b32 v35, v95, v31
	ds_bpermute_b32 v36, v95, v32
	ds_bpermute_b32 v37, v95, v33
	s_waitcnt vmcnt(3) lgkmcnt(8)
	v_mfma_f32_16x16x32_f16 v[50:53], v[54:57], v[102:105], v[50:53]
	global_store_dwordx4 v[92:93], v[30:33], off offset:192
	v_cvt_pk_fp8_f32 v29, v58, v59 op_sel:[0,0,1]
	v_lshlrev_b64 v[54:55], 7, v[90:91]
	s_waitcnt vmcnt(3) lgkmcnt(4)
	v_mfma_f32_16x16x32_f16 v[30:33], v[46:49], v[70:73], v[50:53]
	v_lshl_add_u64 v[46:47], v[84:85], 0, v[54:55]
	global_store_dwordx4 v[46:47], v[62:65], off
	global_store_dwordx4 v[46:47], v[26:29], off offset:64
	s_waitcnt vmcnt(4) lgkmcnt(0)
	s_nop 0
	v_mfma_f32_16x16x32_f16 v[26:29], v[34:37], v[106:109], v[30:33]
	s_and_b64 exec, exec, vcc
	s_cbranch_execz .LBB5_9
	v_mul_u32_u24_e32 v0, 10, v0
	v_ashrrev_i32_e32 v1, 31, v0
	v_lshl_add_u64 v[0:1], v[0:1], 1, v[86:87]
	global_load_dwordx2 v[30:31], v[0:1], off
	s_waitcnt vmcnt(0)
	v_cvt_f32_f16_e32 v32, v30
	v_cvt_f32_f16_sdwa v33, v30 dst_sel:DWORD dst_unused:UNUSED_PAD src0_sel:WORD_1
	v_cvt_f32_f16_e32 v30, v31
	v_cvt_f32_f16_sdwa v31, v31 dst_sel:DWORD dst_unused:UNUSED_PAD src0_sel:WORD_1
	v_pk_add_f32 v[26:27], v[26:27], v[32:33]
	s_nop 0
	v_cvt_pk_f16_f32 v26, v26, v27
	v_pk_add_f32 v[28:29], v[28:29], v[30:31]
	s_nop 0
	v_cvt_pk_f16_f32 v27, v28, v29
	global_store_dwordx2 v[0:1], v[26:27], off
.LBB5_9:
	s_or_b64 exec, exec, s[0:1]
	s_and_saveexec_b64 s[0:1], s[4:5]
	s_cbranch_execz .LBB5_12
	s_nop 2
	ds_read_b128 v[26:29], v96
	s_waitcnt vmcnt(2)
	ds_read_b128 v[30:33], v96 offset:512
	v_cvt_f32_f16_sdwa v55, v42 dst_sel:DWORD dst_unused:UNUSED_PAD src0_sel:WORD_1
	v_cvt_f32_f16_e32 v54, v42
	s_waitcnt vmcnt(1)
	v_lshlrev_b32_e32 v50, 4, v97
	v_or_b32_e32 v0, v50, v94
	s_waitcnt lgkmcnt(0)
	v_fma_mix_f32 v26, v26, v38, v30 op_sel_hi:[0,1,0]
	v_fma_mix_f32 v27, v27, v38, v31 op_sel:[0,1,0] op_sel_hi:[0,1,0]
	v_ashrrev_i32_e32 v1, 31, v0
	v_max_f32_e32 v26, 0, v26
	v_max_f32_e32 v27, 0, v27
	s_waitcnt vmcnt(0)
	v_lshlrev_b64 v[34:35], 8, v[0:1]
	v_pk_add_f32 v[30:31], v[26:27], v[54:55]
	v_cvt_f32_f16_sdwa v27, v43 dst_sel:DWORD dst_unused:UNUSED_PAD src0_sel:WORD_1
	v_cvt_f32_f16_e32 v26, v43
	v_lshl_add_u64 v[52:53], v[82:83], 0, v[34:35]
	ds_read_b128 v[34:37], v96 offset:16
	ds_read_b128 v[46:49], v96 offset:528
	v_fma_mix_f32 v28, v28, v39, v32 op_sel_hi:[0,1,0]
	v_fma_mix_f32 v29, v29, v39, v33 op_sel:[0,1,0] op_sel_hi:[0,1,0]
	v_max_f32_e32 v28, 0, v28
	v_max_f32_e32 v29, 0, v29
	v_pk_add_f32 v[28:29], v[28:29], v[26:27]
	v_cvt_f32_f16_sdwa v27, v44 dst_sel:DWORD dst_unused:UNUSED_PAD src0_sel:WORD_1
	v_cvt_f32_f16_e32 v26, v44
	s_waitcnt lgkmcnt(0)
	v_fma_mix_f32 v32, v34, v40, v46 op_sel_hi:[0,1,0]
	v_fma_mix_f32 v33, v35, v40, v47 op_sel:[0,1,0] op_sel_hi:[0,1,0]
	v_max_f32_e32 v32, 0, v32
	v_max_f32_e32 v33, 0, v33
	v_pk_add_f32 v[32:33], v[32:33], v[26:27]
	v_cvt_f32_f16_sdwa v27, v45 dst_sel:DWORD dst_unused:UNUSED_PAD src0_sel:WORD_1
	v_cvt_f32_f16_e32 v26, v45
	v_fma_mix_f32 v34, v36, v41, v48 op_sel_hi:[0,1,0]
	v_fma_mix_f32 v35, v37, v41, v49 op_sel:[0,1,0] op_sel_hi:[0,1,0]
	v_max_f32_e32 v34, 0, v34
	v_max_f32_e32 v35, 0, v35
	v_pk_add_f32 v[34:35], v[34:35], v[26:27]
	v_mov_b32_e32 v26, 0
	v_cvt_pk_fp8_f32 v26, v30, v31
	v_cvt_pk_f16_f32 v38, v30, v31
	v_cvt_pk_f16_f32 v39, v28, v29
	v_cvt_pk_f16_f32 v40, v32, v33
	v_cvt_pk_f16_f32 v41, v34, v35
	global_store_dwordx4 v[52:53], v[38:41], off
	v_cvt_pk_fp8_f32 v26, v28, v29 op_sel:[0,0,1]
	ds_read_b128 v[28:31], v96 offset:128
	ds_read_b128 v[42:45], v96 offset:640
	v_mov_b32_e32 v27, 0
	v_cvt_f32_f16_sdwa v55, v22 dst_sel:DWORD dst_unused:UNUSED_PAD src0_sel:WORD_1
	v_cvt_f32_f16_e32 v54, v22
	v_cvt_pk_fp8_f32 v27, v32, v33
	s_waitcnt lgkmcnt(0)
	v_fma_mix_f32 v28, v28, v18, v42 op_sel_hi:[0,1,0]
	v_fma_mix_f32 v18, v29, v18, v43 op_sel:[0,1,0] op_sel_hi:[0,1,0]
	v_max_f32_e32 v28, 0, v28
	v_max_f32_e32 v29, 0, v18
	v_pk_add_f32 v[42:43], v[28:29], v[54:55]
	v_cvt_f32_f16_sdwa v29, v23 dst_sel:DWORD dst_unused:UNUSED_PAD src0_sel:WORD_1
	v_cvt_f32_f16_e32 v28, v23
	v_cvt_pk_fp8_f32 v27, v34, v35 op_sel:[0,0,1]
	ds_bpermute_b32 v34, v95, v38
	ds_bpermute_b32 v35, v95, v39
	ds_bpermute_b32 v36, v95, v40
	ds_bpermute_b32 v37, v95, v41
	ds_read_b128 v[38:41], v96 offset:144
	ds_read_b128 v[46:49], v96 offset:656
	v_fma_mix_f32 v22, v30, v19, v44 op_sel_hi:[0,1,0]
	v_fma_mix_f32 v19, v31, v19, v45 op_sel:[0,1,0] op_sel_hi:[0,1,0]
	v_max_f32_e32 v22, 0, v22
	v_max_f32_e32 v23, 0, v19
	v_pk_add_f32 v[22:23], v[22:23], v[28:29]
	v_cvt_f32_f16_sdwa v29, v24 dst_sel:DWORD dst_unused:UNUSED_PAD src0_sel:WORD_1
	v_cvt_f32_f16_e32 v28, v24
	s_waitcnt lgkmcnt(0)
	v_fma_mix_f32 v30, v38, v20, v46 op_sel_hi:[0,1,0]
	v_fma_mix_f32 v20, v39, v20, v47 op_sel:[0,1,0] op_sel_hi:[0,1,0]
	v_fma_mix_f32 v24, v40, v21, v48 op_sel_hi:[0,1,0]
	v_fma_mix_f32 v21, v41, v21, v49 op_sel:[0,1,0] op_sel_hi:[0,1,0]
	v_cvt_f32_f16_sdwa v41, v25 dst_sel:DWORD dst_unused:UNUSED_PAD src0_sel:WORD_1
	v_cvt_f32_f16_e32 v40, v25
	v_max_f32_e32 v30, 0, v30
	v_max_f32_e32 v31, 0, v20
	v_pk_add_f32 v[30:31], v[30:31], v[28:29]
	v_mov_b32_e32 v28, 0
	v_mov_b32_e32 v29, 0
	v_max_f32_e32 v38, 0, v24
	v_max_f32_e32 v39, 0, v21
	v_cvt_pk_fp8_f32 v28, v42, v43
	v_cvt_pk_fp8_f32 v29, v30, v31
	v_pk_add_f32 v[24:25], v[38:39], v[40:41]
	v_cvt_pk_f16_f32 v18, v42, v43
	v_cvt_pk_f16_f32 v19, v22, v23
	v_cvt_pk_f16_f32 v20, v30, v31
	v_cvt_pk_f16_f32 v21, v24, v25
	global_store_dwordx4 v[52:53], v[18:21], off offset:64
	v_cvt_pk_fp8_f32 v28, v22, v23 op_sel:[0,0,1]
	v_cvt_pk_fp8_f32 v29, v24, v25 op_sel:[0,0,1]
	ds_read_b128 v[22:25], v96 offset:256
	ds_read_b128 v[38:41], v96 offset:768
	ds_read_b128 v[42:45], v96 offset:272
	ds_read_b128 v[46:49], v96 offset:784
	global_load_dwordx4 v[54:57], v[88:89], off
	global_load_dwordx4 v[58:61], v[88:89], off offset:1024
	v_cvt_f32_f16_sdwa v31, v14 dst_sel:DWORD dst_unused:UNUSED_PAD src0_sel:WORD_1
	s_waitcnt lgkmcnt(2)
	v_fma_mix_f32 v22, v22, v10, v38 op_sel_hi:[0,1,0]
	v_cvt_f32_f16_e32 v30, v14
	v_fma_mix_f32 v10, v23, v10, v39 op_sel:[0,1,0] op_sel_hi:[0,1,0]
	v_fma_mix_f32 v14, v24, v11, v40 op_sel_hi:[0,1,0]
	v_fma_mix_f32 v11, v25, v11, v41 op_sel:[0,1,0] op_sel_hi:[0,1,0]
	global_load_dwordx4 v[38:41], v[88:89], off offset:2048
	global_load_dwordx4 v[62:65], v[88:89], off offset:3072
	v_max_f32_e32 v22, 0, v22
	v_max_f32_e32 v23, 0, v10
	v_pk_add_f32 v[22:23], v[22:23], v[30:31]
	v_cvt_f32_f16_sdwa v31, v15 dst_sel:DWORD dst_unused:UNUSED_PAD src0_sel:WORD_1
	v_cvt_f32_f16_e32 v30, v15
	v_cvt_f32_f16_sdwa v25, v16 dst_sel:DWORD dst_unused:UNUSED_PAD src0_sel:WORD_1
	v_cvt_f32_f16_e32 v24, v16
	v_max_f32_e32 v14, 0, v14
	v_max_f32_e32 v15, 0, v11
	v_pk_add_f32 v[14:15], v[14:15], v[30:31]
	s_waitcnt lgkmcnt(0)
	v_fma_mix_f32 v30, v42, v12, v46 op_sel_hi:[0,1,0]
	v_fma_mix_f32 v12, v43, v12, v47 op_sel:[0,1,0] op_sel_hi:[0,1,0]
	v_fma_mix_f32 v16, v44, v13, v48 op_sel_hi:[0,1,0]
	v_fma_mix_f32 v13, v45, v13, v49 op_sel:[0,1,0] op_sel_hi:[0,1,0]
	v_cvt_f32_f16_sdwa v45, v17 dst_sel:DWORD dst_unused:UNUSED_PAD src0_sel:WORD_1
	v_cvt_f32_f16_e32 v44, v17
	v_max_f32_e32 v30, 0, v30
	v_max_f32_e32 v31, 0, v12
	v_pk_add_f32 v[24:25], v[30:31], v[24:25]
	v_mov_b32_e32 v30, 0
	v_mov_b32_e32 v31, 0
	v_max_f32_e32 v42, 0, v16
	v_max_f32_e32 v43, 0, v13
	v_cvt_pk_fp8_f32 v30, v22, v23
	v_cvt_pk_fp8_f32 v31, v24, v25
	v_pk_add_f32 v[16:17], v[42:43], v[44:45]
	v_cvt_pk_f16_f32 v10, v22, v23
	v_cvt_pk_f16_f32 v11, v14, v15
	v_cvt_pk_f16_f32 v12, v24, v25
	v_cvt_pk_f16_f32 v13, v16, v17
	global_store_dwordx4 v[52:53], v[10:13], off offset:128
	v_cvt_pk_fp8_f32 v30, v14, v15 op_sel:[0,0,1]
	v_cvt_pk_fp8_f32 v31, v16, v17 op_sel:[0,0,1]
	ds_read_b128 v[14:17], v96 offset:384
	ds_read_b128 v[22:25], v96 offset:896
	ds_read_b128 v[42:45], v96 offset:400
	ds_read_b128 v[46:49], v96 offset:912
	v_cvt_f32_f16_sdwa v67, v6 dst_sel:DWORD dst_unused:UNUSED_PAD src0_sel:WORD_1
	v_cvt_f32_f16_e32 v66, v6
	ds_bpermute_b32 v18, v95, v18
	s_waitcnt lgkmcnt(3)
	v_fma_mix_f32 v14, v14, v2, v22 op_sel_hi:[0,1,0]
	v_fma_mix_f32 v2, v15, v2, v23 op_sel:[0,1,0] op_sel_hi:[0,1,0]
	v_cvt_f32_f16_sdwa v23, v7 dst_sel:DWORD dst_unused:UNUSED_PAD src0_sel:WORD_1
	v_cvt_f32_f16_e32 v22, v7
	v_fma_mix_f32 v6, v16, v3, v24 op_sel_hi:[0,1,0]
	v_fma_mix_f32 v3, v17, v3, v25 op_sel:[0,1,0] op_sel_hi:[0,1,0]
	v_cvt_f32_f16_sdwa v17, v8 dst_sel:DWORD dst_unused:UNUSED_PAD src0_sel:WORD_1
	v_cvt_f32_f16_e32 v16, v8
	v_max_f32_e32 v6, 0, v6
	v_max_f32_e32 v7, 0, v3
	ds_bpermute_b32 v19, v95, v19
	ds_bpermute_b32 v20, v95, v20
	ds_bpermute_b32 v21, v95, v21
	v_pk_add_f32 v[6:7], v[6:7], v[22:23]
	s_waitcnt lgkmcnt(4)
	v_fma_mix_f32 v22, v42, v4, v46 op_sel_hi:[0,1,0]
	v_fma_mix_f32 v4, v43, v4, v47 op_sel:[0,1,0] op_sel_hi:[0,1,0]
	v_max_f32_e32 v22, 0, v22
	v_max_f32_e32 v23, 0, v4
	v_max_f32_e32 v14, 0, v14
	v_max_f32_e32 v15, 0, v2
	v_pk_add_f32 v[16:17], v[22:23], v[16:17]
	v_cvt_f32_f16_sdwa v23, v9 dst_sel:DWORD dst_unused:UNUSED_PAD src0_sel:WORD_1
	v_cvt_f32_f16_e32 v22, v9
	v_pk_add_f32 v[14:15], v[14:15], v[66:67]
	v_mov_b32_e32 v32, 0
	v_mov_b32_e32 v33, 0
	ds_bpermute_b32 v10, v95, v10
	ds_bpermute_b32 v11, v95, v11
	ds_bpermute_b32 v12, v95, v12
	ds_bpermute_b32 v13, v95, v13
	v_fma_mix_f32 v8, v44, v5, v48 op_sel_hi:[0,1,0]
	v_fma_mix_f32 v5, v45, v5, v49 op_sel:[0,1,0] op_sel_hi:[0,1,0]
	v_cvt_pk_fp8_f32 v32, v14, v15
	v_cvt_pk_f16_f32 v2, v14, v15
	v_cvt_pk_f16_f32 v4, v16, v17
	v_max_f32_e32 v8, 0, v8
	v_max_f32_e32 v9, 0, v5
	v_cvt_pk_fp8_f32 v33, v16, v17
	s_waitcnt vmcnt(4)
	v_mfma_f32_16x16x32_f16 v[14:17], v[34:37], v[54:57], 0
	v_add_f32_e64 v22, v8, v22
	v_add_f32_e64 v23, v9, v23
	v_cvt_pk_f16_f32 v3, v6, v7
	v_cvt_pk_f16_f32 v5, v22, v23
	v_cvt_pk_fp8_f32 v32, v6, v7 op_sel:[0,0,1]
	ds_bpermute_b32 v6, v95, v2
	ds_bpermute_b32 v7, v95, v3
	ds_bpermute_b32 v8, v95, v4
	ds_bpermute_b32 v9, v95, v5
	s_waitcnt vmcnt(3) lgkmcnt(8)
	v_mfma_f32_16x16x32_f16 v[14:17], v[18:21], v[58:61], v[14:17]
	global_store_dwordx4 v[52:53], v[2:5], off offset:192
	v_cvt_pk_fp8_f32 v33, v22, v23 op_sel:[0,0,1]
	s_nop 0
	v_lshlrev_b64 v[4:5], 7, v[0:1]
	s_waitcnt vmcnt(3) lgkmcnt(4)
	v_mfma_f32_16x16x32_f16 v[0:3], v[10:13], v[38:41], v[14:17]
	v_lshl_add_u64 v[4:5], v[84:85], 0, v[4:5]
	global_store_dwordx4 v[4:5], v[26:29], off
	global_store_dwordx4 v[4:5], v[30:33], off offset:64
	s_waitcnt vmcnt(4) lgkmcnt(0)
	v_mfma_f32_16x16x32_f16 v[0:3], v[6:9], v[62:65], v[0:3]
	s_and_b64 exec, exec, vcc
	s_cbranch_execz .LBB5_12
	v_mul_u32_u24_e32 v50, 10, v50
	v_ashrrev_i32_e32 v51, 31, v50
	v_lshl_add_u64 v[4:5], v[50:51], 1, v[86:87]
	global_load_dwordx2 v[6:7], v[4:5], off
	s_waitcnt vmcnt(0)
	v_cvt_f32_f16_e32 v8, v6
	v_cvt_f32_f16_sdwa v9, v6 dst_sel:DWORD dst_unused:UNUSED_PAD src0_sel:WORD_1
	v_cvt_f32_f16_e32 v6, v7
	v_cvt_f32_f16_sdwa v7, v7 dst_sel:DWORD dst_unused:UNUSED_PAD src0_sel:WORD_1
	v_pk_add_f32 v[0:1], v[0:1], v[8:9]
	s_nop 0
	v_cvt_pk_f16_f32 v0, v0, v1
	v_pk_add_f32 v[2:3], v[2:3], v[6:7]
	s_nop 0
	v_cvt_pk_f16_f32 v1, v2, v3
	global_store_dwordx2 v[4:5], v[0:1], off

.LBB6_12:
	s_or_b64 exec, exec, s[0:1]
	v_lshrrev_b32_e32 v66, 4, v68
	v_lshlrev_b32_e32 v68, 4, v68
	v_mov_b32_e32 v69, 0
	v_and_b32_e32 v78, 15, v0
	s_waitcnt lgkmcnt(0)
	v_lshl_add_u64 v[70:71], s[20:21], 0, v[68:69]
	v_lshlrev_b32_e32 v68, 4, v78
	v_lshlrev_b32_e32 v68, 1, v68
	v_and_or_b32 v1, v73, 60, v66
	v_lshl_add_u64 v[76:77], s[18:19], 0, v[68:69]
	v_lshlrev_b32_e32 v68, 3, v66
	v_lshlrev_b32_e32 v67, 2, v1
	v_cmp_lt_u32_e64 s[0:1], 9, v78
	v_cmp_eq_u32_e32 vcc, 10, v78
	v_lshlrev_b32_e32 v1, 2, v66
	v_lshl_add_u64 v[68:69], v[76:77], 0, v[68:69]
	v_lshlrev_b32_e32 v66, 2, v78
	v_lshlrev_b32_e32 v75, 2, v75
	s_barrier
	s_and_saveexec_b64 s[12:13], s[4:5]
	s_cbranch_execz .LBB6_19
	ds_read_b128 v[76:79], v75 offset:6144
	ds_read_b128 v[80:83], v75 offset:5632
	ds_read_b128 v[84:87], v75 offset:5648
	s_waitcnt vmcnt(5)
	v_cvt_f32_f16_sdwa v93, v62 dst_sel:DWORD dst_unused:UNUSED_PAD src0_sel:WORD_1
	v_cvt_f32_f16_e32 v92, v62
	ds_read_b128 v[88:91], v75 offset:6160
	s_waitcnt lgkmcnt(2)
	v_fma_mix_f32 v76, v80, v58, v76 op_sel_hi:[0,1,0]
	v_fma_mix_f32 v58, v81, v58, v77 op_sel:[0,1,0] op_sel_hi:[0,1,0]
	v_max_f32_e32 v76, 0, v76
	v_max_f32_e32 v77, 0, v58
	v_pk_add_f32 v[76:77], v[76:77], v[92:93]
	v_fma_mix_f32 v58, v82, v59, v78 op_sel_hi:[0,1,0]
	v_cvt_pk_f16_f32 v80, v76, v77
	v_cvt_f32_f16_sdwa v77, v63 dst_sel:DWORD dst_unused:UNUSED_PAD src0_sel:WORD_1
	v_cvt_f32_f16_e32 v76, v63
	v_fma_mix_f32 v59, v83, v59, v79 op_sel:[0,1,0] op_sel_hi:[0,1,0]
	v_max_f32_e32 v58, 0, v58
	v_max_f32_e32 v59, 0, v59
	v_pk_add_f32 v[58:59], v[58:59], v[76:77]
	s_waitcnt lgkmcnt(0)
	v_fma_mix_f32 v62, v84, v60, v88 op_sel_hi:[0,1,0]
	v_cvt_pk_f16_f32 v76, v58, v59
	v_cvt_f32_f16_sdwa v59, v64 dst_sel:DWORD dst_unused:UNUSED_PAD src0_sel:WORD_1
	v_cvt_f32_f16_e32 v58, v64
	v_fma_mix_f32 v60, v85, v60, v89 op_sel:[0,1,0] op_sel_hi:[0,1,0]
	v_max_f32_e32 v62, 0, v62
	v_max_f32_e32 v63, 0, v60
	v_pk_add_f32 v[58:59], v[62:63], v[58:59]
	v_fma_mix_f32 v60, v86, v61, v90 op_sel_hi:[0,1,0]
	v_cvt_pk_f16_f32 v81, v58, v59
	v_cvt_f32_f16_sdwa v59, v65 dst_sel:DWORD dst_unused:UNUSED_PAD src0_sel:WORD_1
	v_cvt_f32_f16_e32 v58, v65
	v_fma_mix_f32 v61, v87, v61, v91 op_sel:[0,1,0] op_sel_hi:[0,1,0]
	v_max_f32_e32 v60, 0, v60
	v_max_f32_e32 v61, 0, v61
	v_pk_add_f32 v[58:59], v[60:61], v[58:59]
	s_waitcnt vmcnt(4)
	v_cvt_f32_f16_sdwa v89, v54 dst_sel:DWORD dst_unused:UNUSED_PAD src0_sel:WORD_1
	v_cvt_pk_f16_f32 v61, v58, v59
	ds_bpermute_b32 v59, v67, v76
	ds_read_b128 v[62:65], v75 offset:5760
	ds_read_b128 v[76:79], v75 offset:6272
	v_cvt_f32_f16_e32 v88, v54
	ds_bpermute_b32 v58, v67, v80
	ds_bpermute_b32 v60, v67, v81
	ds_read_b128 v[80:83], v75 offset:5776
	ds_read_b128 v[84:87], v75 offset:6288
	s_waitcnt lgkmcnt(4)
	v_fma_mix_f32 v62, v62, v50, v76 op_sel_hi:[0,1,0]
	v_fma_mix_f32 v50, v63, v50, v77 op_sel:[0,1,0] op_sel_hi:[0,1,0]
	v_max_f32_e32 v62, 0, v62
	v_max_f32_e32 v63, 0, v50
	v_pk_add_f32 v[62:63], v[62:63], v[88:89]
	v_fma_mix_f32 v50, v64, v51, v78 op_sel_hi:[0,1,0]
	v_cvt_pk_f16_f32 v76, v62, v63
	v_cvt_f32_f16_sdwa v63, v55 dst_sel:DWORD dst_unused:UNUSED_PAD src0_sel:WORD_1
	v_cvt_f32_f16_e32 v62, v55
	v_fma_mix_f32 v51, v65, v51, v79 op_sel:[0,1,0] op_sel_hi:[0,1,0]
	v_max_f32_e32 v50, 0, v50
	v_max_f32_e32 v51, 0, v51
	v_pk_add_f32 v[50:51], v[50:51], v[62:63]
	s_waitcnt lgkmcnt(0)
	v_fma_mix_f32 v54, v80, v52, v84 op_sel_hi:[0,1,0]
	v_cvt_pk_f16_f32 v62, v50, v51
	v_cvt_f32_f16_sdwa v51, v56 dst_sel:DWORD dst_unused:UNUSED_PAD src0_sel:WORD_1
	v_cvt_f32_f16_e32 v50, v56
	v_fma_mix_f32 v52, v81, v52, v85 op_sel:[0,1,0] op_sel_hi:[0,1,0]
	v_max_f32_e32 v54, 0, v54
	v_max_f32_e32 v55, 0, v52
	v_pk_add_f32 v[50:51], v[54:55], v[50:51]
	v_fma_mix_f32 v52, v82, v53, v86 op_sel_hi:[0,1,0]
	v_cvt_pk_f16_f32 v63, v50, v51
	v_cvt_f32_f16_sdwa v51, v57 dst_sel:DWORD dst_unused:UNUSED_PAD src0_sel:WORD_1
	v_cvt_f32_f16_e32 v50, v57
	global_load_dwordx4 v[54:57], v[70:71], off
	v_fma_mix_f32 v53, v83, v53, v87 op_sel:[0,1,0] op_sel_hi:[0,1,0]
	v_max_f32_e32 v52, 0, v52
	v_max_f32_e32 v53, 0, v53
	v_pk_add_f32 v[50:51], v[52:53], v[50:51]
	ds_bpermute_b32 v52, v67, v63
	v_cvt_pk_f16_f32 v53, v50, v51
	ds_bpermute_b32 v50, v67, v76
	global_load_dwordx4 v[76:79], v[70:71], off offset:1024
	ds_bpermute_b32 v51, v67, v62
	ds_read_b128 v[62:65], v75 offset:5888
	ds_read_b128 v[84:87], v75 offset:5904
	ds_read_b128 v[80:83], v75 offset:6400
	ds_read_b128 v[92:95], v75 offset:6416
	global_load_dwordx4 v[88:91], v[70:71], off offset:2048
	s_waitcnt vmcnt(4)
	v_cvt_f32_f16_sdwa v97, v46 dst_sel:DWORD dst_unused:UNUSED_PAD src0_sel:WORD_1
	v_cvt_f32_f16_e32 v96, v46
	s_waitcnt lgkmcnt(1)
	v_fma_mix_f32 v62, v62, v42, v80 op_sel_hi:[0,1,0]
	v_fma_mix_f32 v42, v63, v42, v81 op_sel:[0,1,0] op_sel_hi:[0,1,0]
	v_max_f32_e32 v62, 0, v62
	v_max_f32_e32 v63, 0, v42
	v_pk_add_f32 v[62:63], v[62:63], v[96:97]
	global_load_dwordx4 v[96:99], v[70:71], off offset:3072
	v_cvt_pk_f16_f32 v80, v62, v63
	v_cvt_f32_f16_sdwa v63, v47 dst_sel:DWORD dst_unused:UNUSED_PAD src0_sel:WORD_1
	v_cvt_f32_f16_e32 v62, v47
	v_fma_mix_f32 v42, v64, v43, v82 op_sel_hi:[0,1,0]
	v_fma_mix_f32 v43, v65, v43, v83 op_sel:[0,1,0] op_sel_hi:[0,1,0]
	v_max_f32_e32 v42, 0, v42
	v_max_f32_e32 v43, 0, v43
	v_pk_add_f32 v[42:43], v[42:43], v[62:63]
	s_waitcnt lgkmcnt(0)
	v_fma_mix_f32 v46, v84, v44, v92 op_sel_hi:[0,1,0]
	v_cvt_pk_f16_f32 v62, v42, v43
	v_cvt_f32_f16_sdwa v43, v48 dst_sel:DWORD dst_unused:UNUSED_PAD src0_sel:WORD_1
	v_cvt_f32_f16_e32 v42, v48
	v_fma_mix_f32 v44, v85, v44, v93 op_sel:[0,1,0] op_sel_hi:[0,1,0]
	v_max_f32_e32 v46, 0, v46
	v_max_f32_e32 v47, 0, v44
	v_pk_add_f32 v[42:43], v[46:47], v[42:43]
	v_fma_mix_f32 v44, v86, v45, v94 op_sel_hi:[0,1,0]
	v_cvt_pk_f16_f32 v81, v42, v43
	v_cvt_f32_f16_sdwa v43, v49 dst_sel:DWORD dst_unused:UNUSED_PAD src0_sel:WORD_1
	v_cvt_f32_f16_e32 v42, v49
	v_fma_mix_f32 v45, v87, v45, v95 op_sel:[0,1,0] op_sel_hi:[0,1,0]
	v_max_f32_e32 v44, 0, v44
	v_max_f32_e32 v45, 0, v45
	v_pk_add_f32 v[42:43], v[44:45], v[42:43]
	s_waitcnt vmcnt(4)
	v_cvt_f32_f16_sdwa v93, v38 dst_sel:DWORD dst_unused:UNUSED_PAD src0_sel:WORD_1
	v_cvt_pk_f16_f32 v45, v42, v43
	ds_bpermute_b32 v43, v67, v62
	ds_read_b128 v[46:49], v75 offset:6016
	ds_read_b128 v[62:65], v75 offset:6528
	v_cvt_f32_f16_e32 v92, v38
	ds_bpermute_b32 v61, v67, v61
	ds_bpermute_b32 v42, v67, v80
	ds_bpermute_b32 v44, v67, v81
	s_waitcnt lgkmcnt(3)
	v_fma_mix_f32 v46, v46, v34, v62 op_sel_hi:[0,1,0]
	v_fma_mix_f32 v34, v47, v34, v63 op_sel:[0,1,0] op_sel_hi:[0,1,0]
	v_max_f32_e32 v46, 0, v46
	v_max_f32_e32 v47, 0, v34
	v_pk_add_f32 v[46:47], v[46:47], v[92:93]
	ds_read_b128 v[80:83], v75 offset:6032
	ds_read_b128 v[84:87], v75 offset:6544
	v_cvt_pk_f16_f32 v62, v46, v47
	v_cvt_f32_f16_sdwa v47, v39 dst_sel:DWORD dst_unused:UNUSED_PAD src0_sel:WORD_1
	v_cvt_f32_f16_e32 v46, v39
	v_fma_mix_f32 v34, v48, v35, v64 op_sel_hi:[0,1,0]
	v_fma_mix_f32 v35, v49, v35, v65 op_sel:[0,1,0] op_sel_hi:[0,1,0]
	v_max_f32_e32 v34, 0, v34
	v_max_f32_e32 v35, 0, v35
	v_pk_add_f32 v[34:35], v[34:35], v[46:47]
	ds_bpermute_b32 v53, v67, v53
	v_cvt_pk_f16_f32 v48, v34, v35
	v_cvt_f32_f16_sdwa v35, v40 dst_sel:DWORD dst_unused:UNUSED_PAD src0_sel:WORD_1
	v_cvt_f32_f16_e32 v34, v40
	s_waitcnt lgkmcnt(1)
	v_fma_mix_f32 v38, v80, v36, v84 op_sel_hi:[0,1,0]
	v_fma_mix_f32 v36, v81, v36, v85 op_sel:[0,1,0] op_sel_hi:[0,1,0]
	v_max_f32_e32 v38, 0, v38
	v_max_f32_e32 v39, 0, v36
	v_cvt_f32_f16_sdwa v47, v41 dst_sel:DWORD dst_unused:UNUSED_PAD src0_sel:WORD_1
	v_cvt_f32_f16_e32 v46, v41
	v_pk_add_f32 v[34:35], v[38:39], v[34:35]
	ds_bpermute_b32 v45, v67, v45
	v_cvt_pk_f16_f32 v40, v34, v35
	v_fma_mix_f32 v34, v82, v37, v86 op_sel_hi:[0,1,0]
	v_fma_mix_f32 v39, v83, v37, v87 op_sel:[0,1,0] op_sel_hi:[0,1,0]
	v_max_f32_e32 v38, 0, v34
	s_waitcnt vmcnt(3)
	v_mfma_f32_16x16x32_f16 v[34:37], v[58:61], v[54:57], 0
	v_max_f32_e32 v39, 0, v39
	v_pk_add_f32 v[38:39], v[38:39], v[46:47]
	ds_bpermute_b32 v40, v67, v40
	v_cvt_pk_f16_f32 v41, v38, v39
	ds_bpermute_b32 v38, v67, v62
	ds_bpermute_b32 v39, v67, v48
	ds_bpermute_b32 v41, v67, v41
	s_waitcnt vmcnt(2) lgkmcnt(5)
	v_mfma_f32_16x16x32_f16 v[34:37], v[50:53], v[76:79], v[34:37]
	s_waitcnt vmcnt(1) lgkmcnt(4)
	v_mfma_f32_16x16x32_f16 v[34:37], v[42:45], v[88:91], v[34:37]
	s_waitcnt vmcnt(0) lgkmcnt(0)
	v_mfma_f32_16x16x32_f16 v[34:37], v[38:41], v[96:99], v[34:37]
	s_and_saveexec_b64 s[4:5], s[0:1]
	s_xor_b64 s[4:5], exec, s[4:5]
	s_cbranch_execz .LBB6_17
	s_and_saveexec_b64 s[14:15], vcc
	s_cbranch_execz .LBB6_16
	s_nop 2
	v_lshl_or_b32 v34, v74, 4, v1
	v_ashrrev_i32_e32 v35, 31, v34
	v_lshl_add_u64 v[34:35], v[34:35], 2, s[8:9]
	global_load_dwordx4 v[34:37], v[34:35], off
	v_mov_b32_e32 v38, 0x1000
	s_waitcnt vmcnt(0)
	v_mul_lo_u32 v34, v34, 44
	v_mul_lo_u32 v35, v35, 44
	v_mul_lo_u32 v36, v36, 44
	ds_add_u32 v34, v38 offset:40
	ds_add_u32 v35, v38 offset:40
	ds_add_u32 v36, v38 offset:40
	v_mul_lo_u32 v34, v37, 44
	ds_add_u32 v34, v38 offset:40

.LBB6_17:
	s_andn2_saveexec_b64 s[4:5], s[4:5]
	s_cbranch_execz .LBB6_19
	v_lshlrev_b32_e32 v38, 4, v74
	v_ashrrev_i32_e32 v39, 31, v38
	v_mul_u32_u24_e32 v40, 10, v38
	v_mov_b32_e32 v41, 0
	v_lshl_add_u64 v[40:41], v[40:41], 1, v[68:69]
	global_load_dwordx2 v[42:43], v[40:41], off
	v_or_b32_e32 v38, v38, v1
	v_ashrrev_i32_e32 v39, 31, v38
	v_lshl_add_u64 v[38:39], v[38:39], 2, s[8:9]
	global_load_dwordx4 v[38:41], v[38:39], off
	s_waitcnt vmcnt(1)
	v_cvt_f32_f16_e32 v46, v42
	v_cvt_f32_f16_sdwa v47, v42 dst_sel:DWORD dst_unused:UNUSED_PAD src0_sel:WORD_1
	v_cvt_f32_f16_e32 v48, v43
	v_cvt_f32_f16_sdwa v49, v43 dst_sel:DWORD dst_unused:UNUSED_PAD src0_sel:WORD_1
	v_add_f32_e32 v34, v34, v46
	v_add_f32_e32 v35, v35, v47
	v_mul_f32_e32 v34, 0x45800000, v34
	v_add_f32_e32 v36, v36, v48
	v_add_f32_e32 v37, v37, v49
	v_mul_f32_e32 v35, 0x45800000, v35
	v_rndne_f32_e32 v34, v34
	v_mul_f32_e32 v36, 0x45800000, v36
	v_mul_f32_e32 v37, 0x45800000, v37
	v_rndne_f32_e32 v35, v35
	v_cvt_i32_f32_e32 v34, v34
	v_rndne_f32_e32 v36, v36
	v_rndne_f32_e32 v37, v37
	v_cvt_i32_f32_e32 v35, v35
	v_cvt_i32_f32_e32 v36, v36
	v_cvt_i32_f32_e32 v37, v37
	s_waitcnt vmcnt(0)
	v_mad_u64_u32 v[42:43], s[4:5], v38, 44, v[66:67]
	v_mad_u64_u32 v[38:39], s[4:5], v39, 44, v[66:67]
	v_mad_u64_u32 v[44:45], s[4:5], v40, 44, v[66:67]
	ds_add_u32 v42, v34
	ds_add_u32 v38, v35
	ds_add_u32 v44, v36
	v_mad_u64_u32 v[34:35], s[4:5], v41, 44, v[66:67]
	ds_add_u32 v34, v37

.LBB6_24:
	s_andn2_saveexec_b64 s[0:1], s[0:1]
	s_cbranch_execz .LBB6_26
	v_lshlrev_b32_e32 v6, 4, v72
	v_ashrrev_i32_e32 v7, 31, v6
	v_mul_u32_u24_e32 v8, 10, v6
	v_mov_b32_e32 v9, 0
	v_lshl_add_u64 v[8:9], v[8:9], 1, v[68:69]
	global_load_dwordx2 v[10:11], v[8:9], off
	v_or_b32_e32 v6, v6, v1
	v_ashrrev_i32_e32 v7, 31, v6
	v_lshl_add_u64 v[6:7], v[6:7], 2, s[8:9]
	global_load_dwordx4 v[6:9], v[6:7], off
	s_waitcnt vmcnt(1)
	v_cvt_f32_f16_e32 v1, v10
	v_cvt_f32_f16_sdwa v14, v10 dst_sel:DWORD dst_unused:UNUSED_PAD src0_sel:WORD_1
	v_cvt_f32_f16_e32 v15, v11
	v_cvt_f32_f16_sdwa v16, v11 dst_sel:DWORD dst_unused:UNUSED_PAD src0_sel:WORD_1
	v_add_f32_e32 v1, v2, v1
	v_add_f32_e32 v2, v3, v14
	v_mul_f32_e32 v1, 0x45800000, v1
	v_add_f32_e32 v3, v4, v15
	v_add_f32_e32 v4, v5, v16
	v_mul_f32_e32 v2, 0x45800000, v2
	v_rndne_f32_e32 v1, v1
	v_mul_f32_e32 v3, 0x45800000, v3
	v_mul_f32_e32 v4, 0x45800000, v4
	v_rndne_f32_e32 v2, v2
	v_cvt_i32_f32_e32 v1, v1
	v_rndne_f32_e32 v3, v3
	v_rndne_f32_e32 v4, v4
	v_cvt_i32_f32_e32 v2, v2
	v_cvt_i32_f32_e32 v3, v3
	v_cvt_i32_f32_e32 v4, v4
	s_waitcnt vmcnt(0)
	v_mad_u64_u32 v[10:11], s[0:1], v6, 44, v[66:67]
	v_mad_u64_u32 v[6:7], s[0:1], v7, 44, v[66:67]
	v_mad_u64_u32 v[12:13], s[0:1], v8, 44, v[66:67]
	ds_add_u32 v10, v1
	ds_add_u32 v6, v2
	ds_add_u32 v12, v3
	v_mad_u64_u32 v[2:3], s[0:1], v9, 44, v[66:67]
	ds_add_u32 v2, v4
